# prep2 balance: scan-B workgroups (bid<16) skip the K-rope rows, others share them; on top of final candidate A
# speedup vs baseline: 1.0085x; 1.0033x over previous
; __device__ __forceinline__ unsigned pk2(float lo, float hi) { return f2bf(lo) | (f2bf(hi) << 16); }
; __device__ __forceinline__ void phase_prep2(const Args& a, const Ctx& c0, int l, bool last) {
;     ...
;     for (int row0 = gw * 2; row0 < NR; row0 += NGW * 2) {
;         f32x2 r1[2], r2[2], c1[2], c2[2]; float rk[2];
; #pragma unroll
;         for (int q = 0; q < 2; ++q) { const float* kr = KR + (size_t)(row0 + q) * 64;
;             r1[q] = *(const f32x2*)(kr + 2 * s); r2[q] = *(const f32x2*)(kr + 16 + 2 * s); c1[q] = *(const f32x2*)(kr + 32 + 2 * s); c2[q] = *(const f32x2*)(kr + 48 + 2 * s);
;             rk[q] = RSTDK[(size_t)(row0 + q) * 8 + hh]; }
; #pragma unroll
;         for (int q = 0; q < 2; ++q) { const int row = row0 + q;
;             const bool lat = row < NL; const int b = lat ? (row >> 12) : ((row - NL) >> 8); const int t = lat ? (row & (SEQ - 1)) : ((row - NL) & (CTXL - 1));
;             const int pos = lat ? CTXL + t : t; const size_t hrow = (size_t)(b * NH + hh) * KVLEN + pos;
;             float cr0 = 1.f, sr0 = 0.f, cr1 = 1.f, sr1 = 0.f, cc0 = 1.f, sc0 = 0.f, cc1 = 1.f, sc1 = 0.f;
;             if (lat) { const float pr = (float)(t >> 6), pc = (float)(t & 63);
;                 __sincosf(pr * inv0, &sr0, &cr0); __sincosf(pr * inv1, &sr1, &cr1); __sincosf(pc * inv0, &sc0, &cc0); __sincosf(pc * inv1, &sc1, &cc1); }
;             const f32x2 a1 = r1[q] * rk[q] * g1, a2 = r2[q] * rk[q] * g2, b1 = c1[q] * rk[q] * g3, b2 = c2[q] * rk[q] * g4;
;             bf16* ko = Ko + hrow * DQK;
;             *(unsigned*)(ko + 128 + 2 * s) = pk2(a1.x * cr0 - a2.x * sr0, a1.y * cr1 - a2.y * sr1);
;             *(unsigned*)(ko + 144 + 2 * s) = pk2(a2.x * cr0 + a1.x * sr0, a2.y * cr1 + a1.y * sr1);
;             *(unsigned*)(ko + 160 + 2 * s) = pk2(b1.x * cc0 - b2.x * sc0, b1.y * cc1 - b2.y * sc1);
;             *(unsigned*)(ko + 176 + 2 * s) = pk2(b2.x * cc0 + b1.x * sc0, b2.y * cc1 + b1.y * sc1); }
;     }
.LBB0_1163:
	s_andn2_b64 vcc, exec, s[2:3]
	s_cbranch_vccnz .LBB0_1233
	s_waitcnt lgkmcnt(0)
	v_mov_b32_e32 v23, v0
	v_readlane_b32 s4, v254, 21
	v_readfirstlane_b32 s2, v23
	s_ashr_i32 s2, s2, 5
	v_readlane_b32 s5, v254, 22
	v_readlane_b32 s6, v254, 23
	v_readlane_b32 s7, v254, 24
	s_and_b32 s2, s2, -2
	v_readlane_b32 s3, v252, 49
	s_mov_b64 s[4:5], s[6:7]
	s_add_i32 s6, s2, s3
	s_cmp_lt_u32 s90, 16
	s_cbranch_scc1 .LBB0_1171
	s_addk_i32 s6, 0xff00
	s_cmpk_gt_i32 s6, 0x43ff
	s_cbranch_scc1 .LBB0_1171
	v_readlane_b32 s2, v254, 17
	v_readlane_b32 s3, v254, 18
	s_mul_i32 s12, s2, 0xc0
	s_lshl_b64 s[2:3], s[12:13], 2
	v_lshlrev_b32_e32 v2, 1, v23
	s_add_u32 s2, s58, s2
	v_and_b32_e32 v10, 14, v2
	s_addc_u32 s3, s59, s3
	v_lshlrev_b32_e32 v8, 2, v10
	s_waitcnt lgkmcnt(0)
	global_load_dwordx2 v[2:3], v8, s[2:3] offset:512
	global_load_dwordx2 v[4:5], v8, s[2:3] offset:576
	global_load_dwordx2 v[6:7], v8, s[2:3] offset:640
	s_nop 0
	global_load_dwordx2 v[8:9], v8, s[2:3] offset:704
	v_cvt_f32_ubyte0_e32 v11, v10
	v_mul_f32_e32 v12, 0xbf549a78, v11
	s_mov_b32 s2, 0xc2fc0000
	v_cmp_gt_f32_e32 vcc, s2, v12
	v_mov_b32_e32 v1, 0x42800000
	s_ashr_i32 s7, s6, 31
	v_cndmask_b32_e32 v12, 0, v1, vcc
	v_fmac_f32_e32 v12, 0xbf549a78, v11
	v_exp_f32_e32 v11, v12
	v_or_b32_e32 v12, 1, v10
	v_cvt_f32_ubyte0_e32 v12, v12
	v_mul_f32_e32 v13, 0xbf549a78, v12
	v_cmp_gt_f32_e64 s[2:3], s2, v13
	v_lshlrev_b32_e32 v10, 1, v10
	v_bfe_u32 v35, v23, 3, 3
	v_cndmask_b32_e64 v13, 0, v1, s[2:3]
	v_fmac_f32_e32 v13, 0xbf549a78, v12
	v_exp_f32_e32 v12, v13
	v_not_b32_e32 v1, 63
	v_cndmask_b32_e32 v13, 0, v1, vcc
	v_ldexp_f32 v36, v11, v13
	v_cndmask_b32_e64 v11, 0, v1, s[2:3]
	v_ldexp_f32 v37, v12, v11
	v_mov_b32_e32 v11, v147
	v_lshl_add_u64 v[10:11], s[4:5], 0, v[10:11]
	s_mov_b64 s[2:3], 0x43200000
	v_lshl_add_u64 v[10:11], v[10:11], 0, s[2:3]
	s_lshl_b64 s[2:3], s[6:7], 5
	v_lshl_or_b32 v12, v35, 2, s2
	v_mov_b32_e32 v13, s3
	s_lshl_b64 s[2:3], s[6:7], 8
	v_and_b32_e32 v14, 7, v23
	v_lshl_or_b32 v14, v14, 3, s2
	v_mov_b32_e32 v15, s3
	s_branch .LBB0_1167
.LBB0_1166:
	s_and_b64 s[14:15], s[2:3], exec
	v_pk_mul_f32 v[20:21], v[20:21], v[22:23] op_sel_hi:[1,0]
	s_cselect_b32 s8, s8, s9
	s_and_b32 s7, s7, 0xff
	s_addk_i32 s10, 0x100
	v_pk_mul_f32 v[24:25], v[24:25], v[22:23] op_sel_hi:[1,0]
	v_pk_mul_f32 v[20:21], v[4:5], v[20:21]
	s_and_b64 s[2:3], s[2:3], exec
	v_pk_mul_f32 v[24:25], v[2:3], v[24:25]
	v_pk_mul_f32 v[18:19], v[18:19], v[22:23] op_sel_hi:[1,0]
	v_pk_mul_f32 v[16:17], v[16:17], v[22:23] op_sel_hi:[1,0]
	v_mul_f32_e32 v22, v20, v39
	s_cselect_b32 s2, s10, s7
	v_fma_f32 v22, v24, v38, -v22
	v_mul_f32_e32 v34, v21, v31
	v_lshl_or_b32 v32, s8, 3, v35
	v_mov_b32_e32 v146, s2
	s_movk_i32 s2, 0x1100
	v_fma_f32 v34, v25, v30, -v34
	v_bfe_u32 v40, v22, 16, 1
	v_mad_i64_i32 v[32:33], s[2:3], v32, s2, v[146:147]
	v_add3_u32 v22, v22, v40, s37
	v_bfe_u32 v40, v34, 16, 1
	s_movk_i32 s7, 0x180
	v_lshrrev_b32_e32 v22, 16, v22
	v_add3_u32 v34, v34, v40, s37
	v_mad_u64_u32 v[40:41], s[2:3], v32, s7, v[10:11]
	v_and_or_b32 v22, v34, s33, v22
	v_mad_i32_i24 v41, v33, s7, v41
	global_store_dword v[40:41], v22, off offset:256
	v_mul_f32_e32 v22, v24, v39
	v_fmac_f32_e32 v22, v20, v38
	v_mul_f32_e32 v20, v25, v31
	v_fmac_f32_e32 v20, v21, v30
	v_bfe_u32 v21, v22, 16, 1
	v_add3_u32 v21, v22, v21, s37
	v_bfe_u32 v22, v20, 16, 1
	v_lshrrev_b32_e32 v21, 16, v21
	v_add3_u32 v20, v20, v22, s37
	v_pk_mul_f32 v[16:17], v[8:9], v[16:17]
	v_and_or_b32 v20, v20, s33, v21
	v_pk_mul_f32 v[18:19], v[6:7], v[18:19]
	global_store_dword v[40:41], v20, off offset:288
	v_mul_f32_e32 v20, v16, v27
	s_nop 0
	v_fma_f32 v20, v18, v26, -v20
	v_mul_f32_e32 v18, v18, v27
	s_nop 0
	v_mul_f32_e32 v21, v17, v29
	v_fmac_f32_e32 v18, v16, v26
	v_mul_f32_e32 v16, v19, v29
	s_addk_i32 s6, 0xf00
	s_mov_b32 s2, 0x1e000
	v_fma_f32 v21, v19, v28, -v21
	v_bfe_u32 v22, v20, 16, 1
	v_fmac_f32_e32 v16, v17, v28
	v_bfe_u32 v17, v18, 16, 1
	s_mov_b32 s3, 0
	v_add3_u32 v20, v20, v22, s37
	v_bfe_u32 v22, v21, 16, 1
	v_add3_u32 v17, v18, v17, s37
	v_bfe_u32 v18, v16, 16, 1
	v_lshl_add_u64 v[12:13], v[12:13], 0, s[2:3]
	s_mov_b32 s2, 0xf0000
	v_lshrrev_b32_e32 v20, 16, v20
	v_add3_u32 v21, v21, v22, s37
	v_lshrrev_b32_e32 v17, 16, v17
	v_add3_u32 v16, v16, v18, s37
	s_mov_b32 s3, 0
	v_and_or_b32 v20, v21, s33, v20
	v_and_or_b32 v16, v16, s33, v17
	s_cmpk_gt_i32 s6, 0x43ff
	v_lshl_add_u64 v[14:15], v[14:15], 0, s[2:3]
	global_store_dword v[40:41], v20, off offset:320
	global_store_dword v[40:41], v16, off offset:352
	s_cbranch_scc1 .LBB0_1171
